# speedup vs baseline: 1.0295x; 1.0073x over previous
.LBB4_15:
	ds_read_b128 v[156:159], v138
	ds_read_b128 v[160:163], v139
	ds_read_b128 v[164:167], v140
	ds_read_b128 v[168:171], v141
	ds_read_b128 v[172:175], v142
	ds_read_b128 v[176:179], v143
	ds_read_b128 v[180:183], v144
	ds_read_b128 v[184:187], v145
	ds_read_b64_tr_b16 v[188:189], v146
	ds_read_b64_tr_b16 v[190:191], v146 offset:512
	ds_read_b64_tr_b16 v[192:193], v147
	ds_read_b64_tr_b16 v[194:195], v147 offset:512
	s_add_i32 s40, s37, -2
	s_min_u32 s41, s37, 0x83
	s_add_i32 s42, s2, 0xffffc000
	s_mov_b32 m0, s18
	s_add_i32 s60, s16, s37
	s_add_i32 s60, s60, -1
	s_cmp_lt_u32 s60, 16
	s_cselect_b32 s61, s54, s55
	s_cselect_b32 s62, 0x20000, s63
	s_lshl_b32 s60, s60, 13
	s_add_i32 s56, s61, s60
	s_add_i32 s57, s56, s62
	s_add_i32 s58, s57, s62
	s_add_i32 s59, s58, s62
	buffer_load_dwordx4 v1, s[8:11], s56 offen lds
	ds_read_b64_tr_b16 v[196:197], v146 offset:4096
	ds_read_b64_tr_b16 v[198:199], v146 offset:4608
	ds_read_b64_tr_b16 v[200:201], v147 offset:4096
	ds_read_b64_tr_b16 v[202:203], v147 offset:4608
	s_mov_b32 m0, s38
	s_nop 0
	buffer_load_dwordx4 v1, s[8:11], s57 offen lds
	ds_read_b64_tr_b16 v[204:205], v222
	ds_read_b64_tr_b16 v[206:207], v222 offset:512
	ds_read_b64_tr_b16 v[208:209], v223
	ds_read_b64_tr_b16 v[210:211], v223 offset:512
	s_mov_b32 m0, s19
	s_nop 0
	buffer_load_dwordx4 v1, s[8:11], s58 offen lds
	ds_read_b64_tr_b16 v[212:213], v222 offset:4096
	ds_read_b64_tr_b16 v[214:215], v222 offset:4608
	ds_read_b64_tr_b16 v[216:217], v223 offset:4096
	ds_read_b64_tr_b16 v[218:219], v223 offset:4608
	s_mov_b32 m0, s39
	s_nop 0
	buffer_load_dwordx4 v1, s[8:11], s59 offen lds
	s_waitcnt lgkmcnt(15)
	s_barrier
	s_waitcnt lgkmcnt(0)
	s_setprio 1
	s_waitcnt lgkmcnt(7)
	v_mfma_f32_16x16x32_bf16 v[126:129], v[188:191], v[156:159], v[126:129]
	v_mfma_f32_16x16x32_bf16 v[94:97], v[188:191], v[164:167], v[94:97]
	s_waitcnt lgkmcnt(6)
	v_mfma_f32_16x16x32_bf16 v[122:125], v[192:195], v[156:159], v[122:125]
	v_mfma_f32_16x16x32_bf16 v[90:93], v[192:195], v[164:167], v[90:93]
	s_waitcnt lgkmcnt(3)
	v_mfma_f32_16x16x32_bf16 v[118:121], v[204:207], v[156:159], v[118:121]
	v_mfma_f32_16x16x32_bf16 v[86:89], v[204:207], v[164:167], v[86:89]
	s_waitcnt lgkmcnt(2)
	v_mfma_f32_16x16x32_bf16 v[114:117], v[208:211], v[156:159], v[114:117]
	v_mfma_f32_16x16x32_bf16 v[82:85], v[208:211], v[164:167], v[82:85]
	v_mfma_f32_16x16x32_bf16 v[126:129], v[196:199], v[160:163], v[126:129]
	v_mfma_f32_16x16x32_bf16 v[94:97], v[196:199], v[168:171], v[94:97]
	v_mfma_f32_16x16x32_bf16 v[122:125], v[200:203], v[160:163], v[122:125]
	v_mfma_f32_16x16x32_bf16 v[90:93], v[200:203], v[168:171], v[90:93]
	s_waitcnt lgkmcnt(1)
	v_mfma_f32_16x16x32_bf16 v[118:121], v[212:215], v[160:163], v[118:121]
	v_mfma_f32_16x16x32_bf16 v[86:89], v[212:215], v[168:171], v[86:89]
	s_waitcnt lgkmcnt(0)
	v_mfma_f32_16x16x32_bf16 v[114:117], v[216:219], v[160:163], v[114:117]
	v_mfma_f32_16x16x32_bf16 v[82:85], v[216:219], v[168:171], v[82:85]
	s_setprio 0
	s_setprio 1
	v_mfma_f32_16x16x32_bf16 v[62:65], v[188:191], v[172:175], v[62:65]
	v_mfma_f32_16x16x32_bf16 v[34:37], v[188:191], v[180:183], v[34:37]
	v_mfma_f32_16x16x32_bf16 v[58:61], v[192:195], v[172:175], v[58:61]
	v_mfma_f32_16x16x32_bf16 v[30:33], v[192:195], v[180:183], v[30:33]
	v_mfma_f32_16x16x32_bf16 v[54:57], v[204:207], v[172:175], v[54:57]
	v_mfma_f32_16x16x32_bf16 v[22:25], v[204:207], v[180:183], v[22:25]
	v_mfma_f32_16x16x32_bf16 v[50:53], v[208:211], v[172:175], v[50:53]
	v_mfma_f32_16x16x32_bf16 v[18:21], v[208:211], v[180:183], v[18:21]
	v_mfma_f32_16x16x32_bf16 v[62:65], v[196:199], v[176:179], v[62:65]
	v_mfma_f32_16x16x32_bf16 v[34:37], v[196:199], v[184:187], v[34:37]
	v_mfma_f32_16x16x32_bf16 v[58:61], v[200:203], v[176:179], v[58:61]
	v_mfma_f32_16x16x32_bf16 v[30:33], v[200:203], v[184:187], v[30:33]
	v_mfma_f32_16x16x32_bf16 v[54:57], v[212:215], v[176:179], v[54:57]
	v_mfma_f32_16x16x32_bf16 v[22:25], v[212:215], v[184:187], v[22:25]
	v_mfma_f32_16x16x32_bf16 v[50:53], v[216:219], v[176:179], v[50:53]
	v_mfma_f32_16x16x32_bf16 v[18:21], v[216:219], v[184:187], v[18:21]
	s_setprio 0
	s_barrier
	ds_read_b64_tr_b16 v[188:189], v146 offset:16384
	ds_read_b64_tr_b16 v[190:191], v146 offset:16896
	ds_read_b64_tr_b16 v[192:193], v147 offset:16384
	ds_read_b64_tr_b16 v[194:195], v147 offset:16896
	s_lshl_b32 s42, s41, 18
	s_or_b32 s43, s42, s23
	s_mov_b32 m0, s17
	s_lshl_b32 s43, s43, 1
	buffer_load_dwordx4 v130, s[4:7], s43 offen lds
	ds_read_b64_tr_b16 v[196:197], v146 offset:20480
	ds_read_b64_tr_b16 v[198:199], v146 offset:20992
	ds_read_b64_tr_b16 v[200:201], v147 offset:20480
	ds_read_b64_tr_b16 v[202:203], v147 offset:20992
	s_mov_b32 m0, s22
	s_or_b32 s42, s42, s24
	buffer_load_dwordx4 v133, s[4:7], s43 offen lds
	ds_read_b64_tr_b16 v[204:205], v222 offset:16384
	ds_read_b64_tr_b16 v[206:207], v222 offset:16896
	ds_read_b64_tr_b16 v[208:209], v223 offset:16384
	ds_read_b64_tr_b16 v[210:211], v223 offset:16896
	s_lshl_b32 s42, s42, 1
	s_mov_b32 m0, s25
	s_nop 0
	buffer_load_dwordx4 v130, s[4:7], s42 offen lds
	ds_read_b64_tr_b16 v[212:213], v222 offset:20480
	ds_read_b64_tr_b16 v[214:215], v222 offset:20992
	ds_read_b64_tr_b16 v[216:217], v223 offset:20480
	ds_read_b64_tr_b16 v[218:219], v223 offset:20992
	s_mov_b32 m0, s26
	s_nop 0
	buffer_load_dwordx4 v133, s[4:7], s42 offen lds
	s_waitcnt lgkmcnt(0)
	s_waitcnt vmcnt(4)
	s_barrier
	s_setprio 1
	s_waitcnt lgkmcnt(7)
	v_mfma_f32_16x16x32_bf16 v[110:113], v[188:191], v[156:159], v[110:113]
	v_mfma_f32_16x16x32_bf16 v[78:81], v[188:191], v[164:167], v[78:81]
	s_waitcnt lgkmcnt(6)
	v_mfma_f32_16x16x32_bf16 v[106:109], v[192:195], v[156:159], v[106:109]
	v_mfma_f32_16x16x32_bf16 v[74:77], v[192:195], v[164:167], v[74:77]
	s_waitcnt lgkmcnt(3)
	v_mfma_f32_16x16x32_bf16 v[102:105], v[204:207], v[156:159], v[102:105]
	v_mfma_f32_16x16x32_bf16 v[70:73], v[204:207], v[164:167], v[70:73]
	s_waitcnt lgkmcnt(2)
	v_mfma_f32_16x16x32_bf16 v[98:101], v[208:211], v[156:159], v[98:101]
	v_mfma_f32_16x16x32_bf16 v[66:69], v[208:211], v[164:167], v[66:69]
	v_mfma_f32_16x16x32_bf16 v[110:113], v[196:199], v[160:163], v[110:113]
	v_mfma_f32_16x16x32_bf16 v[78:81], v[196:199], v[168:171], v[78:81]
	v_mfma_f32_16x16x32_bf16 v[106:109], v[200:203], v[160:163], v[106:109]
	v_mfma_f32_16x16x32_bf16 v[74:77], v[200:203], v[168:171], v[74:77]
	s_waitcnt lgkmcnt(1)
	v_mfma_f32_16x16x32_bf16 v[102:105], v[212:215], v[160:163], v[102:105]
	v_mfma_f32_16x16x32_bf16 v[70:73], v[212:215], v[168:171], v[70:73]
	s_waitcnt lgkmcnt(0)
	v_mfma_f32_16x16x32_bf16 v[98:101], v[216:219], v[160:163], v[98:101]
	v_mfma_f32_16x16x32_bf16 v[66:69], v[216:219], v[168:171], v[66:69]
	s_setprio 0
	s_setprio 1
	v_mfma_f32_16x16x32_bf16 v[46:49], v[188:191], v[172:175], v[46:49]
	v_mfma_f32_16x16x32_bf16 v[10:13], v[188:191], v[180:183], v[10:13]
	v_mfma_f32_16x16x32_bf16 v[38:41], v[192:195], v[172:175], v[38:41]
	v_mfma_f32_16x16x32_bf16 v[2:5], v[192:195], v[180:183], v[2:5]
	v_mfma_f32_16x16x32_bf16 v[26:29], v[204:207], v[172:175], v[26:29]
	v_mfma_f32_16x16x32_bf16 v[14:17], v[204:207], v[180:183], v[14:17]
	v_mfma_f32_16x16x32_bf16 v[42:45], v[208:211], v[172:175], v[42:45]
	v_mfma_f32_16x16x32_bf16 v[6:9], v[208:211], v[180:183], v[6:9]
	v_mfma_f32_16x16x32_bf16 v[46:49], v[196:199], v[176:179], v[46:49]
	v_mfma_f32_16x16x32_bf16 v[10:13], v[196:199], v[184:187], v[10:13]
	v_mfma_f32_16x16x32_bf16 v[38:41], v[200:203], v[176:179], v[38:41]
	v_mfma_f32_16x16x32_bf16 v[2:5], v[200:203], v[184:187], v[2:5]
	v_mfma_f32_16x16x32_bf16 v[26:29], v[212:215], v[176:179], v[26:29]
	v_mfma_f32_16x16x32_bf16 v[14:17], v[212:215], v[184:187], v[14:17]
	v_mfma_f32_16x16x32_bf16 v[42:45], v[216:219], v[176:179], v[42:45]
	v_mfma_f32_16x16x32_bf16 v[6:9], v[216:219], v[184:187], v[6:9]
	s_setprio 0
	s_barrier
	ds_read_b128 v[156:159], v148
	ds_read_b128 v[160:163], v149
	ds_read_b128 v[164:167], v150
	ds_read_b128 v[168:171], v151
	ds_read_b128 v[172:175], v152
	ds_read_b128 v[176:179], v153
	ds_read_b128 v[180:183], v154
	ds_read_b128 v[184:187], v155
	ds_read_b64_tr_b16 v[188:189], v146 offset:32768
	ds_read_b64_tr_b16 v[190:191], v146 offset:33280
	ds_read_b64_tr_b16 v[192:193], v147 offset:32768
	ds_read_b64_tr_b16 v[194:195], v147 offset:33280
	s_lshl_b32 s41, s41, 16
	s_or_b32 s42, s41, s28
	s_mov_b32 m0, s3
	s_lshl_b32 s42, s42, 1
	s_min_u32 s60, s37, 0x83
	s_add_i32 s60, s60, s16
	s_cmp_lt_u32 s60, 16
	s_cselect_b32 s61, s54, s55
	s_cselect_b32 s62, 0x20000, s63
	s_lshl_b32 s60, s60, 13
	s_add_i32 s56, s61, s60
	s_add_i32 s57, s56, s62
	s_add_i32 s58, s57, s62
	s_add_i32 s59, s58, s62
	buffer_load_dwordx4 v1, s[8:11], s56 offen lds
	ds_read_b64_tr_b16 v[196:197], v146 offset:36864
	ds_read_b64_tr_b16 v[198:199], v146 offset:37376
	ds_read_b64_tr_b16 v[200:201], v147 offset:36864
	ds_read_b64_tr_b16 v[202:203], v147 offset:37376
	s_mov_b32 m0, s27
	s_or_b32 s41, s41, s29
	buffer_load_dwordx4 v1, s[8:11], s57 offen lds
	ds_read_b64_tr_b16 v[204:205], v222 offset:32768
	ds_read_b64_tr_b16 v[206:207], v222 offset:33280
	ds_read_b64_tr_b16 v[208:209], v223 offset:32768
	ds_read_b64_tr_b16 v[210:211], v223 offset:33280
	s_lshl_b32 s41, s41, 1
	s_mov_b32 m0, s30
	s_nop 0
	buffer_load_dwordx4 v1, s[8:11], s58 offen lds
	ds_read_b64_tr_b16 v[212:213], v222 offset:36864
	ds_read_b64_tr_b16 v[214:215], v222 offset:37376
	ds_read_b64_tr_b16 v[216:217], v223 offset:36864
	ds_read_b64_tr_b16 v[218:219], v223 offset:37376
	s_mov_b32 m0, s31
	s_nop 0
	buffer_load_dwordx4 v1, s[8:11], s59 offen lds
	s_waitcnt lgkmcnt(15)
	s_barrier
	s_waitcnt lgkmcnt(0)
	s_setprio 1
	s_waitcnt lgkmcnt(7)
	v_mfma_f32_16x16x32_bf16 v[126:129], v[188:191], v[156:159], v[126:129]
	v_mfma_f32_16x16x32_bf16 v[94:97], v[188:191], v[164:167], v[94:97]
	s_waitcnt lgkmcnt(6)
	v_mfma_f32_16x16x32_bf16 v[122:125], v[192:195], v[156:159], v[122:125]
	v_mfma_f32_16x16x32_bf16 v[90:93], v[192:195], v[164:167], v[90:93]
	s_waitcnt lgkmcnt(3)
	v_mfma_f32_16x16x32_bf16 v[118:121], v[204:207], v[156:159], v[118:121]
	v_mfma_f32_16x16x32_bf16 v[86:89], v[204:207], v[164:167], v[86:89]
	s_waitcnt lgkmcnt(2)
	v_mfma_f32_16x16x32_bf16 v[114:117], v[208:211], v[156:159], v[114:117]
	v_mfma_f32_16x16x32_bf16 v[82:85], v[208:211], v[164:167], v[82:85]
	v_mfma_f32_16x16x32_bf16 v[126:129], v[196:199], v[160:163], v[126:129]
	v_mfma_f32_16x16x32_bf16 v[94:97], v[196:199], v[168:171], v[94:97]
	v_mfma_f32_16x16x32_bf16 v[122:125], v[200:203], v[160:163], v[122:125]
	v_mfma_f32_16x16x32_bf16 v[90:93], v[200:203], v[168:171], v[90:93]
	s_waitcnt lgkmcnt(1)
	v_mfma_f32_16x16x32_bf16 v[118:121], v[212:215], v[160:163], v[118:121]
	v_mfma_f32_16x16x32_bf16 v[86:89], v[212:215], v[168:171], v[86:89]
	s_waitcnt lgkmcnt(0)
	v_mfma_f32_16x16x32_bf16 v[114:117], v[216:219], v[160:163], v[114:117]
	v_mfma_f32_16x16x32_bf16 v[82:85], v[216:219], v[168:171], v[82:85]
	s_setprio 0
	s_setprio 1
	v_mfma_f32_16x16x32_bf16 v[62:65], v[188:191], v[172:175], v[62:65]
	v_mfma_f32_16x16x32_bf16 v[34:37], v[188:191], v[180:183], v[34:37]
	v_mfma_f32_16x16x32_bf16 v[58:61], v[192:195], v[172:175], v[58:61]
	v_mfma_f32_16x16x32_bf16 v[30:33], v[192:195], v[180:183], v[30:33]
	v_mfma_f32_16x16x32_bf16 v[54:57], v[204:207], v[172:175], v[54:57]
	v_mfma_f32_16x16x32_bf16 v[22:25], v[204:207], v[180:183], v[22:25]
	v_mfma_f32_16x16x32_bf16 v[50:53], v[208:211], v[172:175], v[50:53]
	v_mfma_f32_16x16x32_bf16 v[18:21], v[208:211], v[180:183], v[18:21]
	v_mfma_f32_16x16x32_bf16 v[62:65], v[196:199], v[176:179], v[62:65]
	v_mfma_f32_16x16x32_bf16 v[34:37], v[196:199], v[184:187], v[34:37]
	v_mfma_f32_16x16x32_bf16 v[58:61], v[200:203], v[176:179], v[58:61]
	v_mfma_f32_16x16x32_bf16 v[30:33], v[200:203], v[184:187], v[30:33]
	v_mfma_f32_16x16x32_bf16 v[54:57], v[212:215], v[176:179], v[54:57]
	v_mfma_f32_16x16x32_bf16 v[22:25], v[212:215], v[184:187], v[22:25]
	v_mfma_f32_16x16x32_bf16 v[50:53], v[216:219], v[176:179], v[50:53]
	v_mfma_f32_16x16x32_bf16 v[18:21], v[216:219], v[184:187], v[18:21]
	s_setprio 0
	s_barrier
	ds_read_b64_tr_b16 v[188:189], v146 offset:49152
	ds_read_b64_tr_b16 v[190:191], v146 offset:49664
	ds_read_b64_tr_b16 v[192:193], v147 offset:49152
	ds_read_b64_tr_b16 v[194:195], v147 offset:49664
	s_min_u32 s41, s40, 0x80
	s_lshl_b32 s41, s41, 18
	s_add_i32 s41, s41, 0xc0000
	s_or_b32 s42, s41, s23
	s_mov_b32 m0, s33
	s_lshl_b32 s42, s42, 1
	buffer_load_dwordx4 v130, s[4:7], s42 offen lds
	ds_read_b64_tr_b16 v[196:197], v146 offset:53248
	ds_read_b64_tr_b16 v[198:199], v146 offset:53760
	ds_read_b64_tr_b16 v[200:201], v147 offset:53248
	ds_read_b64_tr_b16 v[202:203], v147 offset:53760
	s_mov_b32 m0, s34
	s_or_b32 s41, s41, s24
	buffer_load_dwordx4 v133, s[4:7], s42 offen lds
	ds_read_b64_tr_b16 v[204:205], v222 offset:49152
	ds_read_b64_tr_b16 v[206:207], v222 offset:49664
	ds_read_b64_tr_b16 v[208:209], v223 offset:49152
	ds_read_b64_tr_b16 v[210:211], v223 offset:49664
	s_lshl_b32 s41, s41, 1
	s_mov_b32 m0, s35
	s_nop 0
	buffer_load_dwordx4 v130, s[4:7], s41 offen lds
	ds_read_b64_tr_b16 v[212:213], v222 offset:53248
	ds_read_b64_tr_b16 v[214:215], v222 offset:53760
	ds_read_b64_tr_b16 v[216:217], v223 offset:53248
	ds_read_b64_tr_b16 v[218:219], v223 offset:53760
	s_mov_b32 m0, s36
	s_nop 0
	buffer_load_dwordx4 v133, s[4:7], s41 offen lds
	s_waitcnt lgkmcnt(0)
	s_waitcnt vmcnt(4)
	s_barrier
	s_setprio 1
	s_waitcnt lgkmcnt(7)
	v_mfma_f32_16x16x32_bf16 v[110:113], v[188:191], v[156:159], v[110:113]
	v_mfma_f32_16x16x32_bf16 v[78:81], v[188:191], v[164:167], v[78:81]
	s_waitcnt lgkmcnt(6)
	v_mfma_f32_16x16x32_bf16 v[106:109], v[192:195], v[156:159], v[106:109]
	v_mfma_f32_16x16x32_bf16 v[74:77], v[192:195], v[164:167], v[74:77]
	s_waitcnt lgkmcnt(3)
	v_mfma_f32_16x16x32_bf16 v[102:105], v[204:207], v[156:159], v[102:105]
	v_mfma_f32_16x16x32_bf16 v[70:73], v[204:207], v[164:167], v[70:73]
	s_waitcnt lgkmcnt(2)
	v_mfma_f32_16x16x32_bf16 v[98:101], v[208:211], v[156:159], v[98:101]
	v_mfma_f32_16x16x32_bf16 v[66:69], v[208:211], v[164:167], v[66:69]
	v_mfma_f32_16x16x32_bf16 v[110:113], v[196:199], v[160:163], v[110:113]
	v_mfma_f32_16x16x32_bf16 v[78:81], v[196:199], v[168:171], v[78:81]
	v_mfma_f32_16x16x32_bf16 v[106:109], v[200:203], v[160:163], v[106:109]
	v_mfma_f32_16x16x32_bf16 v[74:77], v[200:203], v[168:171], v[74:77]
	s_waitcnt lgkmcnt(1)
	v_mfma_f32_16x16x32_bf16 v[102:105], v[212:215], v[160:163], v[102:105]
	v_mfma_f32_16x16x32_bf16 v[70:73], v[212:215], v[168:171], v[70:73]
	s_waitcnt lgkmcnt(0)
	v_mfma_f32_16x16x32_bf16 v[98:101], v[216:219], v[160:163], v[98:101]
	v_mfma_f32_16x16x32_bf16 v[66:69], v[216:219], v[168:171], v[66:69]
	s_setprio 0
	s_setprio 1
	v_mfma_f32_16x16x32_bf16 v[46:49], v[188:191], v[172:175], v[46:49]
	v_mfma_f32_16x16x32_bf16 v[10:13], v[188:191], v[180:183], v[10:13]
	v_mfma_f32_16x16x32_bf16 v[38:41], v[192:195], v[172:175], v[38:41]
	v_mfma_f32_16x16x32_bf16 v[2:5], v[192:195], v[180:183], v[2:5]
	v_mfma_f32_16x16x32_bf16 v[26:29], v[204:207], v[172:175], v[26:29]
	v_mfma_f32_16x16x32_bf16 v[14:17], v[204:207], v[180:183], v[14:17]
	v_mfma_f32_16x16x32_bf16 v[42:45], v[208:211], v[172:175], v[42:45]
	v_mfma_f32_16x16x32_bf16 v[6:9], v[208:211], v[180:183], v[6:9]
	v_mfma_f32_16x16x32_bf16 v[46:49], v[196:199], v[176:179], v[46:49]
	v_mfma_f32_16x16x32_bf16 v[10:13], v[196:199], v[184:187], v[10:13]
	v_mfma_f32_16x16x32_bf16 v[38:41], v[200:203], v[176:179], v[38:41]
	v_mfma_f32_16x16x32_bf16 v[2:5], v[200:203], v[184:187], v[2:5]
	v_mfma_f32_16x16x32_bf16 v[26:29], v[212:215], v[176:179], v[26:29]
	v_mfma_f32_16x16x32_bf16 v[14:17], v[212:215], v[184:187], v[14:17]
	v_mfma_f32_16x16x32_bf16 v[42:45], v[216:219], v[176:179], v[42:45]
	v_mfma_f32_16x16x32_bf16 v[6:9], v[216:219], v[184:187], v[6:9]
	s_setprio 0
	s_barrier
	s_add_i32 s41, s16, s37
	s_add_i32 s44, s41, -2
	s_cmpk_lt_u32 s40, 0x82
	s_cselect_b64 s[42:43], -1, 0
	s_cmp_gt_i32 s44, 13
	s_cselect_b64 s[44:45], -1, 0
	s_and_b64 s[42:43], s[42:43], s[44:45]
	s_andn2_b64 vcc, exec, s[42:43]
	s_cbranch_vccnz .LBB4_14
	s_add_i32 s41, s41, -16
	s_and_b32 s41, s41, 62
	s_cmp_lg_u32 s41, 0
	s_cbranch_scc1 .LBB4_14
	ds_read2_b32 v[156:157], v137 offset1:16
	ds_read2_b32 v[158:159], v137 offset0:128 offset1:144
	s_waitcnt lgkmcnt(1)
	v_pk_mul_f32 v[128:129], v[156:157], v[128:129] op_sel_hi:[0,1]
	v_pk_mul_f32 v[126:127], v[156:157], v[126:127] op_sel_hi:[0,1]
	v_pk_mul_f32 v[124:125], v[156:157], v[124:125] op_sel_hi:[0,1]
	v_pk_mul_f32 v[122:123], v[156:157], v[122:123] op_sel_hi:[0,1]
	v_pk_mul_f32 v[120:121], v[156:157], v[120:121] op_sel_hi:[0,1]
	v_pk_mul_f32 v[118:119], v[156:157], v[118:119] op_sel_hi:[0,1]
	v_pk_mul_f32 v[116:117], v[156:157], v[116:117] op_sel_hi:[0,1]
	v_pk_mul_f32 v[114:115], v[156:157], v[114:115] op_sel_hi:[0,1]
	v_pk_mul_f32 v[112:113], v[156:157], v[112:113] op_sel_hi:[0,1]
	v_pk_mul_f32 v[110:111], v[156:157], v[110:111] op_sel_hi:[0,1]
	v_pk_mul_f32 v[108:109], v[156:157], v[108:109] op_sel_hi:[0,1]
	v_pk_mul_f32 v[106:107], v[156:157], v[106:107] op_sel_hi:[0,1]
	v_pk_mul_f32 v[104:105], v[156:157], v[104:105] op_sel_hi:[0,1]
	v_pk_mul_f32 v[102:103], v[156:157], v[102:103] op_sel_hi:[0,1]
	v_pk_mul_f32 v[100:101], v[156:157], v[100:101] op_sel_hi:[0,1]
	v_pk_mul_f32 v[98:99], v[156:157], v[98:99] op_sel_hi:[0,1]
	v_mov_b32_e32 v156, v157
	v_pk_mul_f32 v[96:97], v[156:157], v[96:97] op_sel_hi:[0,1]
	v_pk_mul_f32 v[94:95], v[156:157], v[94:95] op_sel_hi:[0,1]
	v_pk_mul_f32 v[92:93], v[156:157], v[92:93] op_sel_hi:[0,1]
	v_pk_mul_f32 v[90:91], v[156:157], v[90:91] op_sel_hi:[0,1]
	v_pk_mul_f32 v[88:89], v[156:157], v[88:89] op_sel_hi:[0,1]
	v_pk_mul_f32 v[86:87], v[156:157], v[86:87] op_sel_hi:[0,1]
	v_pk_mul_f32 v[84:85], v[156:157], v[84:85] op_sel_hi:[0,1]
	v_pk_mul_f32 v[82:83], v[156:157], v[82:83] op_sel_hi:[0,1]
	v_pk_mul_f32 v[80:81], v[156:157], v[80:81] op_sel_hi:[0,1]
	v_pk_mul_f32 v[78:79], v[156:157], v[78:79] op_sel_hi:[0,1]
	v_pk_mul_f32 v[76:77], v[156:157], v[76:77] op_sel_hi:[0,1]
	v_pk_mul_f32 v[74:75], v[156:157], v[74:75] op_sel_hi:[0,1]
	v_pk_mul_f32 v[72:73], v[156:157], v[72:73] op_sel_hi:[0,1]
	v_pk_mul_f32 v[70:71], v[156:157], v[70:71] op_sel_hi:[0,1]
	v_pk_mul_f32 v[68:69], v[156:157], v[68:69] op_sel_hi:[0,1]
	v_pk_mul_f32 v[66:67], v[156:157], v[66:67] op_sel_hi:[0,1]
	s_waitcnt lgkmcnt(0)
	v_mov_b32_e32 v156, v159
	v_pk_mul_f32 v[64:65], v[158:159], v[64:65] op_sel_hi:[0,1]
	v_pk_mul_f32 v[62:63], v[158:159], v[62:63] op_sel_hi:[0,1]
	v_pk_mul_f32 v[60:61], v[158:159], v[60:61] op_sel_hi:[0,1]
	v_pk_mul_f32 v[58:59], v[158:159], v[58:59] op_sel_hi:[0,1]
	v_pk_mul_f32 v[56:57], v[158:159], v[56:57] op_sel_hi:[0,1]
	v_pk_mul_f32 v[54:55], v[158:159], v[54:55] op_sel_hi:[0,1]
	v_pk_mul_f32 v[52:53], v[158:159], v[52:53] op_sel_hi:[0,1]
	v_pk_mul_f32 v[50:51], v[158:159], v[50:51] op_sel_hi:[0,1]
	v_pk_mul_f32 v[48:49], v[158:159], v[48:49] op_sel_hi:[0,1]
	v_pk_mul_f32 v[46:47], v[158:159], v[46:47] op_sel_hi:[0,1]
	v_pk_mul_f32 v[40:41], v[158:159], v[40:41] op_sel_hi:[0,1]
	v_pk_mul_f32 v[38:39], v[158:159], v[38:39] op_sel_hi:[0,1]
	v_pk_mul_f32 v[28:29], v[158:159], v[28:29] op_sel_hi:[0,1]
	v_pk_mul_f32 v[26:27], v[158:159], v[26:27] op_sel_hi:[0,1]
	v_pk_mul_f32 v[44:45], v[158:159], v[44:45] op_sel_hi:[0,1]
	v_pk_mul_f32 v[42:43], v[158:159], v[42:43] op_sel_hi:[0,1]
	v_pk_mul_f32 v[36:37], v[156:157], v[36:37] op_sel_hi:[0,1]
	v_pk_mul_f32 v[34:35], v[156:157], v[34:35] op_sel_hi:[0,1]
	v_pk_mul_f32 v[32:33], v[156:157], v[32:33] op_sel_hi:[0,1]
	v_pk_mul_f32 v[30:31], v[156:157], v[30:31] op_sel_hi:[0,1]
	v_pk_mul_f32 v[24:25], v[156:157], v[24:25] op_sel_hi:[0,1]
	v_pk_mul_f32 v[22:23], v[156:157], v[22:23] op_sel_hi:[0,1]
	v_pk_mul_f32 v[20:21], v[156:157], v[20:21] op_sel_hi:[0,1]
	v_pk_mul_f32 v[18:19], v[156:157], v[18:19] op_sel_hi:[0,1]
	v_pk_mul_f32 v[12:13], v[156:157], v[12:13] op_sel_hi:[0,1]
	v_pk_mul_f32 v[10:11], v[156:157], v[10:11] op_sel_hi:[0,1]
	v_pk_mul_f32 v[4:5], v[156:157], v[4:5] op_sel_hi:[0,1]
	v_pk_mul_f32 v[2:3], v[156:157], v[2:3] op_sel_hi:[0,1]
	v_pk_mul_f32 v[16:17], v[156:157], v[16:17] op_sel_hi:[0,1]
	v_pk_mul_f32 v[14:15], v[156:157], v[14:15] op_sel_hi:[0,1]
	v_pk_mul_f32 v[8:9], v[156:157], v[8:9] op_sel_hi:[0,1]
	v_pk_mul_f32 v[6:7], v[156:157], v[6:7] op_sel_hi:[0,1]
	s_branch .LBB4_14
